# cache-policy: final output stores made non-temporal
# speedup vs baseline: 1.0046x; 1.0046x over previous
.LBB0_1977:
	v_ashrrev_i32_e32 v66, 12, v72
	v_and_b32_e32 v67, 0xffc, v72
	s_waitcnt vmcnt(7)
	v_ashrrev_i32_e32 v49, 31, v44
	v_mov_b32_e32 v48, v44
	v_ashrrev_i32_e32 v51, 31, v45
	v_mov_b32_e32 v50, v45
	v_ashrrev_i32_e32 v45, 31, v46
	v_mov_b32_e32 v44, v46
	v_ashrrev_i32_e32 v53, 31, v47
	v_mov_b32_e32 v52, v47
	s_waitcnt vmcnt(5)
	v_ashrrev_i32_e32 v47, 31, v40
	v_mov_b32_e32 v46, v40
	v_ashrrev_i32_e32 v55, 31, v41
	v_mov_b32_e32 v54, v41
	v_ashrrev_i32_e32 v41, 31, v42
	v_mov_b32_e32 v40, v42
	v_ashrrev_i32_e32 v57, 31, v43
	v_mov_b32_e32 v56, v43
	s_waitcnt vmcnt(3)
	v_ashrrev_i32_e32 v43, 31, v32
	v_mov_b32_e32 v42, v32
	v_ashrrev_i32_e32 v59, 31, v33
	v_mov_b32_e32 v58, v33
	v_ashrrev_i32_e32 v33, 31, v34
	v_mov_b32_e32 v32, v34
	v_mad_i32_i24 v82, v66, s47, v67
	v_add_u32_e32 v80, s78, v72
	v_ashrrev_i32_e32 v61, 31, v35
	v_mov_b32_e32 v60, v35
	s_waitcnt vmcnt(0)
	v_ashrrev_i32_e32 v35, 31, v36
	v_mov_b32_e32 v34, v36
	v_ashrrev_i32_e32 v63, 31, v37
	v_mov_b32_e32 v62, v37
	v_ashrrev_i32_e32 v37, 31, v38
	v_mov_b32_e32 v36, v38
	v_lshlrev_b64 v[116:117], 10, v[32:33]
	v_ashrrev_i32_e32 v83, 31, v82
	v_or_b32_e32 v32, 1, v82
	v_cmp_gt_i32_e64 s[2:3], s71, v80
	v_lshlrev_b64 v[156:157], 10, v[40:41]
	v_lshlrev_b64 v[70:71], 10, v[34:35]
	v_lshlrev_b64 v[66:67], 10, v[36:37]
	v_or_b32_e32 v34, 2, v82
	v_or_b32_e32 v36, 3, v82
	v_lshlrev_b64 v[40:41], 11, v[82:83]
	v_ashrrev_i32_e32 v33, 31, v32
	v_ashrrev_i32_e32 v65, 31, v39
	v_mov_b32_e32 v64, v39
	v_and_b32_e32 v81, 0xfffff000, v72
	v_cndmask_b32_e64 v86, v72, v80, s[2:3]
	v_ashrrev_i32_e32 v35, 31, v34
	v_ashrrev_i32_e32 v37, 31, v36
	v_lshl_add_u64 v[40:41], v[76:77], 0, v[40:41]
	v_lshlrev_b64 v[32:33], 11, v[32:33]
	v_cmp_lt_i32_e32 vcc, s70, v80
	v_lshlrev_b64 v[152:153], 10, v[42:43]
	v_lshlrev_b64 v[96:97], 10, v[64:65]
	v_add_u32_e32 v168, v167, v81
	v_mov_b32_e32 v72, v80
	v_ashrrev_i32_e32 v42, 12, v86
	v_and_b32_e32 v43, 0xffc, v86
	v_lshlrev_b64 v[34:35], 11, v[34:35]
	v_lshlrev_b64 v[36:37], 11, v[36:37]
	global_load_dwordx2 v[64:65], v[40:41], off nt
	global_load_dwordx2 v[80:81], v[40:41], off offset:512 nt
	global_load_dwordx2 v[82:83], v[40:41], off offset:1024 nt
	global_load_dwordx2 v[86:87], v[40:41], off offset:1536 nt
	v_lshl_add_u64 v[32:33], v[76:77], 0, v[32:33]
	s_mov_b32 s10, 35
	v_lshl_add_u64 v[34:35], v[76:77], 0, v[34:35]
	v_lshl_add_u64 v[36:37], v[76:77], 0, v[36:37]
	global_load_dwordx2 v[88:89], v[32:33], off nt
	global_load_dwordx2 v[90:91], v[32:33], off offset:512 nt
	global_load_dwordx2 v[92:93], v[32:33], off offset:1024 nt
	global_load_dwordx2 v[94:95], v[32:33], off offset:1536 nt
	global_load_dwordx2 v[100:101], v[34:35], off nt
	global_load_dwordx2 v[104:105], v[34:35], off offset:512 nt
	global_load_dwordx2 v[108:109], v[34:35], off offset:1024 nt
	global_load_dwordx2 v[112:113], v[34:35], off offset:1536 nt
	global_load_dwordx2 v[174:175], v[36:37], off nt
	global_load_dwordx2 v[176:177], v[36:37], off offset:512 nt
	global_load_dwordx2 v[178:179], v[36:37], off offset:1024 nt
	global_load_dwordx2 v[180:181], v[36:37], off offset:1536 nt
	s_ashr_i32 s11, s10, 31
	s_lshl_b64 s[2:3], s[10:11], 3
	s_add_u32 s2, s0, s2
	s_mov_b32 s14, 35
	s_addc_u32 s3, s1, s3
	s_load_dwordx2 s[2:3], s[2:3], 0x0
	s_ashr_i32 s15, s14, 31
	s_lshl_b64 s[10:11], s[14:15], 3
	s_add_u32 s10, s0, s10
	v_mul_i32_i24_e32 v42, 0x1100, v42
	s_addc_u32 s11, s1, s11
	v_add_lshl_u32 v42, v42, v43, 2
	s_load_dwordx2 s[10:11], s[10:11], 0x0
	v_ashrrev_i32_e32 v43, 31, v42
	v_or_b32_e32 v40, 4, v42
	v_lshlrev_b64 v[32:33], 2, v[42:43]
	v_ashrrev_i32_e32 v41, 31, v40
	v_lshlrev_b64 v[34:35], 2, v[40:41]
	s_waitcnt lgkmcnt(0)
	v_lshl_add_u64 v[40:41], s[2:3], 0, v[32:33]
	v_add_co_u32_e64 v40, s[2:3], s33, v40
	v_lshl_add_u64 v[32:33], s[10:11], 0, v[32:33]
	s_nop 0
	v_addc_co_u32_e64 v41, s[2:3], 0, v41, s[2:3]
	v_lshlrev_b64 v[162:163], 10, v[44:45]
	v_lshlrev_b64 v[158:159], 10, v[46:47]
	v_or_b32_e32 v44, 8, v42
	v_or_b32_e32 v46, 12, v42
	v_add_co_u32_e64 v32, s[2:3], s46, v32
	s_mov_b32 s18, 35
	v_ashrrev_i32_e32 v45, 31, v44
	v_ashrrev_i32_e32 v47, 31, v46
	v_addc_co_u32_e64 v33, s[2:3], 0, v33, s[2:3]
	v_lshlrev_b64 v[84:85], 10, v[48:49]
	v_lshlrev_b64 v[114:115], 10, v[60:61]
	v_lshlrev_b64 v[68:69], 10, v[62:63]
	v_lshlrev_b64 v[36:37], 2, v[44:45]
	v_lshlrev_b64 v[48:49], 2, v[46:47]
	global_load_dwordx4 v[44:47], v[40:41], off
	global_load_dwordx4 v[60:63], v[32:33], off
	s_ashr_i32 s19, s18, 31
	s_lshl_b64 s[2:3], s[18:19], 3
	s_add_u32 s2, s0, s2
	s_mov_b32 s22, 35
	s_addc_u32 s3, s1, s3
	s_load_dwordx2 s[2:3], s[2:3], 0x0
	s_ashr_i32 s23, s22, 31
	s_lshl_b64 s[10:11], s[22:23], 3
	s_add_u32 s10, s0, s10
	s_addc_u32 s11, s1, s11
	s_load_dwordx2 s[10:11], s[10:11], 0x0
	s_waitcnt lgkmcnt(0)
	v_lshl_add_u64 v[32:33], s[2:3], 0, v[34:35]
	v_add_co_u32_e64 v32, s[2:3], s33, v32
	s_mov_b32 s26, 35
	s_nop 0
	v_addc_co_u32_e64 v33, s[2:3], 0, v33, s[2:3]
	global_load_dwordx4 v[40:43], v[32:33], off
	v_lshl_add_u64 v[32:33], s[10:11], 0, v[34:35]
	v_add_co_u32_e64 v32, s[2:3], s46, v32
	v_lshlrev_b64 v[154:155], 10, v[56:57]
	s_nop 0
	v_addc_co_u32_e64 v33, s[2:3], 0, v33, s[2:3]
	v_lshlrev_b64 v[150:151], 10, v[58:59]
	global_load_dwordx4 v[56:59], v[32:33], off
	s_ashr_i32 s27, s26, 31
	s_lshl_b64 s[2:3], s[26:27], 3
	s_add_u32 s2, s0, s2
	s_mov_b32 s36, 35
	s_addc_u32 s3, s1, s3
	s_load_dwordx2 s[2:3], s[2:3], 0x0
	s_ashr_i32 s37, s36, 31
	s_lshl_b64 s[10:11], s[36:37], 3
	s_add_u32 s10, s0, s10
	s_addc_u32 s11, s1, s11
	s_load_dwordx2 s[10:11], s[10:11], 0x0
	s_waitcnt lgkmcnt(0)
	v_lshl_add_u64 v[32:33], s[2:3], 0, v[36:37]
	v_add_co_u32_e64 v32, s[2:3], s33, v32
	s_mov_b32 s42, 35
	s_nop 0
	v_addc_co_u32_e64 v33, s[2:3], 0, v33, s[2:3]
	v_lshl_add_u64 v[36:37], s[10:11], 0, v[36:37]
	v_add_co_u32_e64 v36, s[2:3], s46, v36
	v_lshlrev_b64 v[160:161], 10, v[52:53]
	s_nop 0
	v_addc_co_u32_e64 v37, s[2:3], 0, v37, s[2:3]
	v_lshlrev_b64 v[38:39], 10, v[54:55]
	global_load_dwordx4 v[32:35], v[32:33], off
	s_mov_b32 s52, 35
	global_load_dwordx4 v[52:55], v[36:37], off
	s_ashr_i32 s43, s42, 31
	s_lshl_b64 s[2:3], s[42:43], 3
	s_add_u32 s2, s0, s2
	s_addc_u32 s3, s1, s3
	s_load_dwordx2 s[2:3], s[2:3], 0x0
	s_ashr_i32 s53, s52, 31
	s_lshl_b64 s[10:11], s[52:53], 3
	s_add_u32 s10, s0, s10
	s_addc_u32 s11, s1, s11
	s_load_dwordx2 s[10:11], s[10:11], 0x0
	s_waitcnt lgkmcnt(0)
	v_lshl_add_u64 v[36:37], s[2:3], 0, v[48:49]
	v_add_co_u32_e64 v36, s[2:3], s33, v36
	s_mov_b32 s58, 35
	s_nop 0
	v_addc_co_u32_e64 v37, s[2:3], 0, v37, s[2:3]
	global_load_dwordx4 v[170:173], v[36:37], off
	v_lshl_add_u64 v[36:37], s[10:11], 0, v[48:49]
	v_add_co_u32_e64 v36, s[2:3], s46, v36
	v_lshlrev_b64 v[164:165], 10, v[50:51]
	s_nop 0
	v_addc_co_u32_e64 v37, s[2:3], 0, v37, s[2:3]
	global_load_dwordx4 v[48:51], v[36:37], off
	s_ashr_i32 s59, s58, 31
	s_lshl_b64 s[2:3], s[58:59], 3
	s_add_u32 s2, s0, s2
	s_addc_u32 s3, s1, s3
	s_load_dwordx2 s[2:3], s[2:3], 0x0
	v_lshlrev_b32_e32 v74, 2, v166
	s_waitcnt vmcnt(23)
	v_lshlrev_b32_e32 v118, 16, v64
	v_and_b32_e32 v119, 0xffff0000, v64
	v_lshlrev_b32_e32 v122, 16, v65
	s_waitcnt lgkmcnt(0)
	v_lshl_add_u64 v[36:37], s[2:3], 0, v[84:85]
	v_lshl_add_u64 v[36:37], v[36:37], 0, v[74:75]
	v_and_b32_e32 v123, 0xffff0000, v65
	v_lshl_add_u64 v[64:65], v[36:37], 0, s[8:9]
	v_add_co_u32_e64 v36, s[2:3], s72, v36
	s_mov_b32 s28, 35
	s_nop 0
	v_addc_co_u32_e64 v37, s[2:3], 0, v37, s[2:3]
	s_waitcnt vmcnt(22)
	v_lshlrev_b32_e32 v120, 16, v80
	v_and_b32_e32 v121, 0xffff0000, v80
	v_lshlrev_b32_e32 v126, 16, v81
	v_and_b32_e32 v127, 0xffff0000, v81
	s_waitcnt vmcnt(21)
	v_lshlrev_b32_e32 v124, 16, v82
	v_and_b32_e32 v125, 0xffff0000, v82
	v_lshlrev_b32_e32 v130, 16, v83
	v_and_b32_e32 v131, 0xffff0000, v83
	s_waitcnt vmcnt(11)
	v_lshlrev_b32_e32 v80, 16, v174
	v_and_b32_e32 v81, 0xffff0000, v174
	v_lshlrev_b32_e32 v82, 16, v175
	v_and_b32_e32 v83, 0xffff0000, v175
	s_waitcnt vmcnt(10)
	v_lshlrev_b32_e32 v84, 16, v176
	v_and_b32_e32 v85, 0xffff0000, v176
	global_load_dword v169, v[36:37], off nt
	global_load_dword v174, v[64:65], off offset:256 nt
	global_load_dword v175, v[64:65], off offset:512 nt
	global_load_dword v176, v[64:65], off offset:768 nt
	s_ashr_i32 s29, s28, 31
	s_lshl_b64 s[2:3], s[28:29], 3
	s_add_u32 s2, s0, s2
	s_addc_u32 s3, s1, s3
	s_load_dwordx2 s[2:3], s[2:3], 0x0
	s_mov_b32 s34, 35
	v_lshlrev_b32_e32 v132, 16, v88
	v_and_b32_e32 v133, 0xffff0000, v88
	v_lshlrev_b32_e32 v138, 16, v89
	s_waitcnt lgkmcnt(0)
	v_lshl_add_u64 v[36:37], s[2:3], 0, v[164:165]
	v_lshl_add_u64 v[36:37], v[36:37], 0, v[74:75]
	v_lshl_add_u64 v[64:65], v[36:37], 0, s[8:9]
	v_add_co_u32_e64 v36, s[2:3], s72, v36
	v_and_b32_e32 v139, 0xffff0000, v89
	s_nop 0
	v_addc_co_u32_e64 v37, s[2:3], 0, v37, s[2:3]
	v_lshlrev_b32_e32 v140, 16, v92
	v_and_b32_e32 v141, 0xffff0000, v92
	v_lshlrev_b32_e32 v146, 16, v93
	v_and_b32_e32 v147, 0xffff0000, v93
	v_lshlrev_b32_e32 v88, 16, v177
	v_and_b32_e32 v89, 0xffff0000, v177
	s_waitcnt vmcnt(13)
	v_lshlrev_b32_e32 v92, 16, v179
	v_and_b32_e32 v93, 0xffff0000, v179
	global_load_dword v177, v[36:37], off nt
	global_load_dword v179, v[64:65], off offset:256 nt
	global_load_dword v183, v[64:65], off offset:512 nt
	global_load_dword v187, v[64:65], off offset:768 nt
	s_ashr_i32 s35, s34, 31
	s_lshl_b64 s[2:3], s[34:35], 3
	s_add_u32 s2, s0, s2
	s_addc_u32 s3, s1, s3
	s_load_dwordx2 s[2:3], s[2:3], 0x0
	s_mov_b32 s38, 35
	s_mov_b32 s44, 35
	s_mov_b32 s50, 35
	s_mov_b32 s56, 35
	s_waitcnt lgkmcnt(0)
	v_lshl_add_u64 v[36:37], s[2:3], 0, v[162:163]
	v_lshl_add_u64 v[36:37], v[36:37], 0, v[74:75]
	v_lshl_add_u64 v[64:65], v[36:37], 0, s[8:9]
	v_add_co_u32_e64 v36, s[2:3], s72, v36
	s_mov_b32 s60, 35
	s_nop 0
	v_addc_co_u32_e64 v37, s[2:3], 0, v37, s[2:3]
	global_load_dword v188, v[36:37], off nt
	global_load_dword v189, v[64:65], off offset:256 nt
	global_load_dword v190, v[64:65], off offset:512 nt
	global_load_dword v191, v[64:65], off offset:768 nt
	s_ashr_i32 s39, s38, 31
	s_lshl_b64 s[2:3], s[38:39], 3
	s_add_u32 s2, s0, s2
	s_addc_u32 s3, s1, s3
	s_load_dwordx2 s[2:3], s[2:3], 0x0
	s_mov_b32 s54, 35
	v_lshlrev_b32_e32 v128, 16, v86
	v_and_b32_e32 v129, 0xffff0000, v86
	v_lshlrev_b32_e32 v134, 16, v87
	s_waitcnt lgkmcnt(0)
	v_lshl_add_u64 v[36:37], s[2:3], 0, v[160:161]
	v_lshl_add_u64 v[36:37], v[36:37], 0, v[74:75]
	v_lshl_add_u64 v[64:65], v[36:37], 0, s[8:9]
	v_add_co_u32_e64 v36, s[2:3], s72, v36
	v_and_b32_e32 v135, 0xffff0000, v87
	s_nop 0
	v_addc_co_u32_e64 v37, s[2:3], 0, v37, s[2:3]
	global_load_dword v192, v[36:37], off nt
	global_load_dword v193, v[64:65], off offset:256 nt
	global_load_dword v194, v[64:65], off offset:512 nt
	global_load_dword v195, v[64:65], off offset:768 nt
	s_ashr_i32 s45, s44, 31
	s_lshl_b64 s[2:3], s[44:45], 3
	s_add_u32 s2, s0, s2
	s_addc_u32 s3, s1, s3
	s_load_dwordx2 s[2:3], s[2:3], 0x0
	v_lshlrev_b32_e32 v136, 16, v90
	v_and_b32_e32 v137, 0xffff0000, v90
	v_lshlrev_b32_e32 v142, 16, v91
	v_and_b32_e32 v143, 0xffff0000, v91
	s_waitcnt lgkmcnt(0)
	v_lshl_add_u64 v[36:37], s[2:3], 0, v[158:159]
	v_lshl_add_u64 v[36:37], v[36:37], 0, v[74:75]
	v_lshl_add_u64 v[64:65], v[36:37], 0, s[8:9]
	v_add_co_u32_e64 v36, s[2:3], s72, v36
	s_waitcnt vmcnt(14)
	v_cvt_f32_fp8_sdwa v160, v174 src0_sel:BYTE_2
	v_addc_co_u32_e64 v37, s[2:3], 0, v37, s[2:3]
	global_load_dword v196, v[36:37], off nt
	global_load_dword v197, v[64:65], off offset:256 nt
	global_load_dword v198, v[64:65], off offset:512 nt
	global_load_dword v199, v[64:65], off offset:768 nt
	s_ashr_i32 s51, s50, 31
	s_lshl_b64 s[2:3], s[50:51], 3
	s_add_u32 s2, s0, s2
	s_addc_u32 s3, s1, s3
	s_load_dwordx2 s[2:3], s[2:3], 0x0
	v_cvt_f32_fp8_sdwa v161, v174 src0_sel:BYTE_3
	s_waitcnt vmcnt(17)
	v_cvt_f32_fp8_e32 v162, v175
	v_cvt_f32_fp8_sdwa v163, v175 src0_sel:BYTE_1
	v_cvt_f32_fp8_sdwa v164, v175 src0_sel:BYTE_2
	s_waitcnt lgkmcnt(0)
	v_lshl_add_u64 v[64:65], s[2:3], 0, v[38:39]
	v_lshl_add_u64 v[64:65], v[64:65], 0, v[74:75]
	v_lshl_add_u64 v[158:159], v[64:65], 0, s[8:9]
	v_add_co_u32_e64 v64, s[2:3], s72, v64
	v_cvt_f32_fp8_sdwa v165, v175 src0_sel:BYTE_3
	s_nop 0
	v_addc_co_u32_e64 v65, s[2:3], 0, v65, s[2:3]
	global_load_dword v200, v[64:65], off nt
	global_load_dword v201, v[158:159], off offset:256 nt
	global_load_dword v202, v[158:159], off offset:512 nt
	global_load_dword v203, v[158:159], off offset:768 nt
	s_ashr_i32 s57, s56, 31
	s_lshl_b64 s[2:3], s[56:57], 3
	s_add_u32 s2, s0, s2
	s_addc_u32 s3, s1, s3
	s_load_dwordx2 s[2:3], s[2:3], 0x0
	v_cvt_f32_fp8_e32 v158, v174
	v_cvt_f32_fp8_sdwa v159, v174 src0_sel:BYTE_1
	v_mov_b64_e32 v[36:37], v[170:171]
	v_mov_b64_e32 v[38:39], v[172:173]
	s_waitcnt lgkmcnt(0)
	v_lshl_add_u64 v[64:65], s[2:3], 0, v[156:157]
	v_lshl_add_u64 v[64:65], v[64:65], 0, v[74:75]
	v_lshl_add_u64 v[156:157], v[64:65], 0, s[8:9]
	v_add_co_u32_e64 v64, s[2:3], s72, v64
	s_waitcnt vmcnt(20)
	v_cvt_f32_fp8_e32 v170, v176
	v_addc_co_u32_e64 v65, s[2:3], 0, v65, s[2:3]
	global_load_dword v204, v[64:65], off nt
	global_load_dword v205, v[156:157], off offset:256 nt
	global_load_dword v206, v[156:157], off offset:512 nt
	global_load_dword v207, v[156:157], off offset:768 nt
	s_ashr_i32 s61, s60, 31
	s_lshl_b64 s[2:3], s[60:61], 3
	s_add_u32 s2, s0, s2
	s_addc_u32 s3, s1, s3
	s_load_dwordx2 s[2:3], s[2:3], 0x0
	v_cvt_f32_fp8_e32 v64, v169
	v_cvt_f32_fp8_sdwa v65, v169 src0_sel:BYTE_1
	v_cvt_f32_fp8_sdwa v156, v169 src0_sel:BYTE_2
	v_cvt_f32_fp8_sdwa v157, v169 src0_sel:BYTE_3
	s_waitcnt lgkmcnt(0)
	v_lshl_add_u64 v[154:155], s[2:3], 0, v[154:155]
	v_lshl_add_u64 v[154:155], v[154:155], 0, v[74:75]
	v_lshl_add_u64 v[174:175], v[154:155], 0, s[8:9]
	v_add_co_u32_e64 v154, s[2:3], s72, v154
	v_cvt_f32_fp8_sdwa v171, v176 src0_sel:BYTE_1
	s_nop 0
	v_addc_co_u32_e64 v155, s[2:3], 0, v155, s[2:3]
	global_load_dword v169, v[154:155], off nt
	global_load_dword v208, v[174:175], off offset:256 nt
	global_load_dword v209, v[174:175], off offset:512 nt
	global_load_dword v210, v[174:175], off offset:768 nt
	s_ashr_i32 s55, s54, 31
	s_lshl_b64 s[2:3], s[54:55], 3
	s_add_u32 s2, s0, s2
	s_addc_u32 s3, s1, s3
	v_cvt_f32_fp8_sdwa v172, v176 src0_sel:BYTE_2
	v_cvt_f32_fp8_sdwa v173, v176 src0_sel:BYTE_3
	s_load_dwordx2 s[2:3], s[2:3], 0x0
	v_lshlrev_b32_e32 v144, 16, v94
	v_and_b32_e32 v145, 0xffff0000, v94
	v_lshlrev_b32_e32 v148, 16, v95
	v_and_b32_e32 v149, 0xffff0000, v95
	v_lshlrev_b32_e32 v86, 16, v178
	v_and_b32_e32 v87, 0xffff0000, v178
	v_lshlrev_b32_e32 v90, 16, v180
	v_and_b32_e32 v91, 0xffff0000, v180
	v_lshlrev_b32_e32 v94, 16, v181
	v_and_b32_e32 v95, 0xffff0000, v181
	s_waitcnt vmcnt(27)
	v_cvt_f32_fp8_e32 v154, v177
	v_cvt_f32_fp8_sdwa v155, v177 src0_sel:BYTE_1
	v_cvt_f32_fp8_sdwa v174, v177 src0_sel:BYTE_2
	v_cvt_f32_fp8_sdwa v175, v177 src0_sel:BYTE_3
	s_waitcnt vmcnt(26)
	v_cvt_f32_fp8_e32 v176, v179
	v_cvt_f32_fp8_sdwa v177, v179 src0_sel:BYTE_1
	v_cvt_f32_fp8_sdwa v178, v179 src0_sel:BYTE_2
	v_cvt_f32_fp8_sdwa v179, v179 src0_sel:BYTE_3
	s_waitcnt vmcnt(25)
	v_cvt_f32_fp8_e32 v180, v183
	v_cvt_f32_fp8_sdwa v181, v183 src0_sel:BYTE_1
	v_cvt_f32_fp8_sdwa v182, v183 src0_sel:BYTE_2
	v_cvt_f32_fp8_sdwa v183, v183 src0_sel:BYTE_3
	s_waitcnt vmcnt(24)
	v_cvt_f32_fp8_e32 v184, v187
	v_cvt_f32_fp8_sdwa v185, v187 src0_sel:BYTE_1
	v_cvt_f32_fp8_sdwa v186, v187 src0_sel:BYTE_2
	v_cvt_f32_fp8_sdwa v187, v187 src0_sel:BYTE_3
	v_pk_fma_f32 v[156:157], v[16:17], v[156:157], 0 op_sel_hi:[0,1,0]
	v_pk_fma_f32 v[64:65], v[16:17], v[64:65], 0 op_sel_hi:[0,1,0]
	v_pk_fma_f32 v[160:161], v[16:17], v[160:161], 0 op_sel_hi:[0,1,0]
	v_pk_fma_f32 v[158:159], v[16:17], v[158:159], 0 op_sel_hi:[0,1,0]
	v_pk_fma_f32 v[164:165], v[16:17], v[164:165], 0 op_sel_hi:[0,1,0]
	v_pk_fma_f32 v[162:163], v[16:17], v[162:163], 0 op_sel_hi:[0,1,0]
	v_pk_fma_f32 v[172:173], v[16:17], v[172:173], 0 op_sel_hi:[0,1,0]
	v_pk_fma_f32 v[170:171], v[16:17], v[170:171], 0 op_sel_hi:[0,1,0]
	v_pk_fma_f32 v[64:65], v[16:17], v[154:155], v[64:65] op_sel:[1,0,0]
	v_pk_fma_f32 v[154:155], v[16:17], v[174:175], v[156:157] op_sel:[1,0,0]
	v_pk_fma_f32 v[156:157], v[16:17], v[176:177], v[158:159] op_sel:[1,0,0]
	v_pk_fma_f32 v[158:159], v[16:17], v[178:179], v[160:161] op_sel:[1,0,0]
	v_pk_fma_f32 v[160:161], v[16:17], v[180:181], v[162:163] op_sel:[1,0,0]
	v_pk_fma_f32 v[162:163], v[16:17], v[182:183], v[164:165] op_sel:[1,0,0]
	v_pk_fma_f32 v[164:165], v[16:17], v[184:185], v[170:171] op_sel:[1,0,0]
	v_pk_fma_f32 v[170:171], v[16:17], v[186:187], v[172:173] op_sel:[1,0,0]
	v_mov_b64_e32 v[16:17], v[60:61]
	s_waitcnt lgkmcnt(0)
	v_lshl_add_u64 v[60:61], s[2:3], 0, v[152:153]
	v_lshl_add_u64 v[60:61], v[60:61], 0, v[74:75]
	v_lshl_add_u64 v[152:153], v[60:61], 0, s[8:9]
	v_add_co_u32_e64 v60, s[2:3], s72, v60
	s_mov_b32 s48, 35
	s_nop 0
	v_addc_co_u32_e64 v61, s[2:3], 0, v61, s[2:3]
	global_load_dword v211, v[60:61], off nt
	global_load_dword v212, v[152:153], off offset:256 nt
	global_load_dword v213, v[152:153], off offset:512 nt
	global_load_dword v214, v[152:153], off offset:768 nt
	s_ashr_i32 s49, s48, 31
	s_lshl_b64 s[2:3], s[48:49], 3
	s_add_u32 s2, s0, s2
	s_addc_u32 s3, s1, s3
	s_load_dwordx2 s[2:3], s[2:3], 0x0
	s_waitcnt vmcnt(27)
	v_cvt_f32_fp8_sdwa v152, v188 src0_sel:BYTE_2
	v_cvt_f32_fp8_sdwa v153, v188 src0_sel:BYTE_3
	s_waitcnt vmcnt(26)
	v_cvt_f32_fp8_e32 v172, v189
	v_cvt_f32_fp8_sdwa v173, v189 src0_sel:BYTE_1
	s_waitcnt vmcnt(25)
	v_cvt_f32_fp8_sdwa v178, v190 src0_sel:BYTE_2
	v_cvt_f32_fp8_sdwa v179, v190 src0_sel:BYTE_3
	s_waitcnt vmcnt(24)
	v_cvt_f32_fp8_e32 v180, v191
	v_cvt_f32_fp8_sdwa v181, v191 src0_sel:BYTE_1
	s_waitcnt lgkmcnt(0)
	v_lshl_add_u64 v[150:151], s[2:3], 0, v[150:151]
	v_lshl_add_u64 v[150:151], v[150:151], 0, v[74:75]
	v_pk_fma_f32 v[152:153], v[18:19], v[152:153], v[154:155] op_sel_hi:[0,1,1]
	v_pk_fma_f32 v[154:155], v[18:19], v[172:173], v[156:157] op_sel_hi:[0,1,1]
	v_pk_fma_f32 v[156:157], v[18:19], v[178:179], v[162:163] op_sel_hi:[0,1,1]
	v_pk_fma_f32 v[162:163], v[18:19], v[180:181], v[164:165] op_sel_hi:[0,1,1]
	v_lshl_add_u64 v[164:165], v[150:151], 0, s[8:9]
	v_add_co_u32_e64 v150, s[2:3], s72, v150
	s_mov_b32 s40, 35
	s_nop 0
	v_addc_co_u32_e64 v151, s[2:3], 0, v151, s[2:3]
	global_load_dword v215, v[150:151], off nt
	global_load_dword v216, v[164:165], off offset:256 nt
	global_load_dword v217, v[164:165], off offset:512 nt
	global_load_dword v218, v[164:165], off offset:768 nt
	s_ashr_i32 s41, s40, 31
	s_lshl_b64 s[2:3], s[40:41], 3
	s_add_u32 s2, s0, s2
	v_cvt_f32_fp8_e32 v60, v188
	v_cvt_f32_fp8_sdwa v61, v188 src0_sel:BYTE_1
	v_cvt_f32_fp8_sdwa v174, v189 src0_sel:BYTE_2
	v_cvt_f32_fp8_sdwa v175, v189 src0_sel:BYTE_3
	v_cvt_f32_fp8_e32 v176, v190
	v_cvt_f32_fp8_sdwa v177, v190 src0_sel:BYTE_1
	v_cvt_f32_fp8_sdwa v182, v191 src0_sel:BYTE_2
	v_cvt_f32_fp8_sdwa v183, v191 src0_sel:BYTE_3
	s_addc_u32 s3, s1, s3
	s_load_dwordx2 s[2:3], s[2:3], 0x0
	s_waitcnt vmcnt(27)
	v_cvt_f32_fp8_e32 v150, v192
	v_cvt_f32_fp8_sdwa v151, v192 src0_sel:BYTE_1
	v_pk_fma_f32 v[60:61], v[18:19], v[60:61], v[64:65] op_sel_hi:[0,1,1]
	v_pk_fma_f32 v[64:65], v[18:19], v[174:175], v[158:159] op_sel_hi:[0,1,1]
	v_pk_fma_f32 v[158:159], v[18:19], v[176:177], v[160:161] op_sel_hi:[0,1,1]
	v_pk_fma_f32 v[160:161], v[18:19], v[182:183], v[170:171] op_sel_hi:[0,1,1]
	v_cvt_f32_fp8_sdwa v164, v192 src0_sel:BYTE_2
	v_cvt_f32_fp8_sdwa v165, v192 src0_sel:BYTE_3
	s_waitcnt vmcnt(26)
	v_cvt_f32_fp8_e32 v170, v193
	v_cvt_f32_fp8_sdwa v171, v193 src0_sel:BYTE_1
	v_cvt_f32_fp8_sdwa v172, v193 src0_sel:BYTE_2
	v_cvt_f32_fp8_sdwa v173, v193 src0_sel:BYTE_3
	s_waitcnt vmcnt(25)
	v_cvt_f32_fp8_e32 v174, v194
	v_cvt_f32_fp8_sdwa v175, v194 src0_sel:BYTE_1
	v_cvt_f32_fp8_sdwa v176, v194 src0_sel:BYTE_2
	v_cvt_f32_fp8_sdwa v177, v194 src0_sel:BYTE_3
	s_waitcnt vmcnt(24)
	v_cvt_f32_fp8_e32 v178, v195
	v_cvt_f32_fp8_sdwa v179, v195 src0_sel:BYTE_1
	v_cvt_f32_fp8_sdwa v180, v195 src0_sel:BYTE_2
	v_cvt_f32_fp8_sdwa v181, v195 src0_sel:BYTE_3
	v_pk_fma_f32 v[150:151], v[18:19], v[150:151], v[60:61] op_sel:[1,0,0]
	s_waitcnt lgkmcnt(0)
	v_lshl_add_u64 v[60:61], s[2:3], 0, v[116:117]
	v_lshl_add_u64 v[60:61], v[60:61], 0, v[74:75]
	v_pk_fma_f32 v[152:153], v[18:19], v[164:165], v[152:153] op_sel:[1,0,0]
	v_pk_fma_f32 v[154:155], v[18:19], v[170:171], v[154:155] op_sel:[1,0,0]
	v_pk_fma_f32 v[164:165], v[18:19], v[172:173], v[64:65] op_sel:[1,0,0]
	v_pk_fma_f32 v[158:159], v[18:19], v[174:175], v[158:159] op_sel:[1,0,0]
	v_pk_fma_f32 v[156:157], v[18:19], v[176:177], v[156:157] op_sel:[1,0,0]
	v_pk_fma_f32 v[162:163], v[18:19], v[178:179], v[162:163] op_sel:[1,0,0]
	v_pk_fma_f32 v[160:161], v[18:19], v[180:181], v[160:161] op_sel:[1,0,0]
	v_mov_b64_e32 v[18:19], v[62:63]
	v_lshl_add_u64 v[62:63], v[60:61], 0, s[8:9]
	v_add_co_u32_e64 v60, s[2:3], s72, v60
	s_mov_b32 s30, 35
	s_nop 0
	v_addc_co_u32_e64 v61, s[2:3], 0, v61, s[2:3]
	global_load_dword v219, v[60:61], off nt
	global_load_dword v220, v[62:63], off offset:256 nt
	global_load_dword v221, v[62:63], off offset:512 nt
	global_load_dword v222, v[62:63], off offset:768 nt
	s_ashr_i32 s31, s30, 31
	s_lshl_b64 s[2:3], s[30:31], 3
	s_add_u32 s2, s0, s2
	s_addc_u32 s3, s1, s3
	s_load_dwordx2 s[2:3], s[2:3], 0x0
	s_mov_b32 s24, 35
	s_waitcnt vmcnt(27)
	v_cvt_f32_fp8_e32 v60, v196
	v_cvt_f32_fp8_sdwa v61, v196 src0_sel:BYTE_1
	v_cvt_f32_fp8_sdwa v62, v196 src0_sel:BYTE_2
	s_waitcnt lgkmcnt(0)
	v_lshl_add_u64 v[114:115], s[2:3], 0, v[114:115]
	v_lshl_add_u64 v[114:115], v[114:115], 0, v[74:75]
	v_lshl_add_u64 v[178:179], v[114:115], 0, s[8:9]
	v_add_co_u32_e64 v114, s[2:3], s72, v114
	v_cvt_f32_fp8_sdwa v63, v196 src0_sel:BYTE_3
	s_nop 0
	v_addc_co_u32_e64 v115, s[2:3], 0, v115, s[2:3]
	global_load_dword v223, v[114:115], off nt
	global_load_dword v224, v[178:179], off offset:256 nt
	global_load_dword v225, v[178:179], off offset:512 nt
	global_load_dword v226, v[178:179], off offset:768 nt
	s_ashr_i32 s25, s24, 31
	s_lshl_b64 s[2:3], s[24:25], 3
	s_add_u32 s2, s0, s2
	s_addc_u32 s3, s1, s3
	s_waitcnt vmcnt(30)
	v_cvt_f32_fp8_e32 v64, v197
	v_cvt_f32_fp8_sdwa v65, v197 src0_sel:BYTE_1
	v_cvt_f32_fp8_sdwa v116, v197 src0_sel:BYTE_2
	v_cvt_f32_fp8_sdwa v117, v197 src0_sel:BYTE_3
	s_waitcnt vmcnt(29)
	v_cvt_f32_fp8_e32 v170, v198
	v_cvt_f32_fp8_sdwa v171, v198 src0_sel:BYTE_1
	v_cvt_f32_fp8_sdwa v172, v198 src0_sel:BYTE_2
	v_cvt_f32_fp8_sdwa v173, v198 src0_sel:BYTE_3
	s_waitcnt vmcnt(28)
	v_cvt_f32_fp8_e32 v174, v199
	v_cvt_f32_fp8_sdwa v175, v199 src0_sel:BYTE_1
	v_cvt_f32_fp8_sdwa v176, v199 src0_sel:BYTE_2
	v_cvt_f32_fp8_sdwa v177, v199 src0_sel:BYTE_3
	s_load_dwordx2 s[2:3], s[2:3], 0x0
	s_waitcnt vmcnt(27)
	v_cvt_f32_fp8_e32 v114, v200
	v_cvt_f32_fp8_sdwa v115, v200 src0_sel:BYTE_1
	v_cvt_f32_fp8_sdwa v178, v200 src0_sel:BYTE_2
	v_cvt_f32_fp8_sdwa v179, v200 src0_sel:BYTE_3
	s_waitcnt vmcnt(26)
	v_cvt_f32_fp8_e32 v180, v201
	v_cvt_f32_fp8_sdwa v181, v201 src0_sel:BYTE_1
	v_cvt_f32_fp8_sdwa v182, v201 src0_sel:BYTE_2
	v_cvt_f32_fp8_sdwa v183, v201 src0_sel:BYTE_3
	s_waitcnt vmcnt(25)
	v_cvt_f32_fp8_e32 v184, v202
	v_cvt_f32_fp8_sdwa v185, v202 src0_sel:BYTE_1
	v_cvt_f32_fp8_sdwa v186, v202 src0_sel:BYTE_2
	v_cvt_f32_fp8_sdwa v187, v202 src0_sel:BYTE_3
	s_waitcnt vmcnt(24)
	v_cvt_f32_fp8_e32 v188, v203
	v_cvt_f32_fp8_sdwa v189, v203 src0_sel:BYTE_1
	v_cvt_f32_fp8_sdwa v190, v203 src0_sel:BYTE_2
	v_cvt_f32_fp8_sdwa v191, v203 src0_sel:BYTE_3
	v_pk_fma_f32 v[62:63], v[20:21], v[62:63], 0 op_sel_hi:[0,1,0]
	v_pk_fma_f32 v[60:61], v[20:21], v[60:61], 0 op_sel_hi:[0,1,0]
	v_pk_fma_f32 v[116:117], v[20:21], v[116:117], 0 op_sel_hi:[0,1,0]
	v_pk_fma_f32 v[64:65], v[20:21], v[64:65], 0 op_sel_hi:[0,1,0]
	v_pk_fma_f32 v[172:173], v[20:21], v[172:173], 0 op_sel_hi:[0,1,0]
	v_pk_fma_f32 v[170:171], v[20:21], v[170:171], 0 op_sel_hi:[0,1,0]
	v_pk_fma_f32 v[176:177], v[20:21], v[176:177], 0 op_sel_hi:[0,1,0]
	v_pk_fma_f32 v[174:175], v[20:21], v[174:175], 0 op_sel_hi:[0,1,0]
	v_pk_fma_f32 v[60:61], v[20:21], v[114:115], v[60:61] op_sel:[1,0,0]
	v_pk_fma_f32 v[62:63], v[20:21], v[178:179], v[62:63] op_sel:[1,0,0]
	v_pk_fma_f32 v[64:65], v[20:21], v[180:181], v[64:65] op_sel:[1,0,0]
	v_pk_fma_f32 v[114:115], v[20:21], v[182:183], v[116:117] op_sel:[1,0,0]
	v_pk_fma_f32 v[116:117], v[20:21], v[184:185], v[170:171] op_sel:[1,0,0]
	v_pk_fma_f32 v[170:171], v[20:21], v[186:187], v[172:173] op_sel:[1,0,0]
	v_pk_fma_f32 v[172:173], v[20:21], v[188:189], v[174:175] op_sel:[1,0,0]
	v_pk_fma_f32 v[174:175], v[20:21], v[190:191], v[176:177] op_sel:[1,0,0]
	v_mov_b64_e32 v[20:21], v[56:57]
	s_waitcnt lgkmcnt(0)
	v_lshl_add_u64 v[56:57], s[2:3], 0, v[70:71]
	v_lshl_add_u64 v[56:57], v[56:57], 0, v[74:75]
	v_lshl_add_u64 v[70:71], v[56:57], 0, s[8:9]
	v_add_co_u32_e64 v56, s[2:3], s72, v56
	s_mov_b32 s20, 35
	s_nop 0
	v_addc_co_u32_e64 v57, s[2:3], 0, v57, s[2:3]
	global_load_dword v200, v[56:57], off nt
	global_load_dword v201, v[70:71], off offset:256 nt
	global_load_dword v202, v[70:71], off offset:512 nt
	global_load_dword v203, v[70:71], off offset:768 nt
	s_ashr_i32 s21, s20, 31
	s_lshl_b64 s[2:3], s[20:21], 3
	s_add_u32 s2, s0, s2
	s_addc_u32 s3, s1, s3
	s_load_dwordx2 s[2:3], s[2:3], 0x0
	s_waitcnt vmcnt(27)
	v_cvt_f32_fp8_sdwa v70, v204 src0_sel:BYTE_2
	v_cvt_f32_fp8_sdwa v71, v204 src0_sel:BYTE_3
	s_waitcnt vmcnt(25)
	v_cvt_f32_fp8_sdwa v182, v206 src0_sel:BYTE_2
	v_cvt_f32_fp8_sdwa v183, v206 src0_sel:BYTE_3
	s_waitcnt vmcnt(24)
	v_cvt_f32_fp8_e32 v184, v207
	v_cvt_f32_fp8_sdwa v185, v207 src0_sel:BYTE_1
	s_waitcnt lgkmcnt(0)
	v_lshl_add_u64 v[68:69], s[2:3], 0, v[68:69]
	v_lshl_add_u64 v[68:69], v[68:69], 0, v[74:75]
	v_pk_fma_f32 v[62:63], v[22:23], v[70:71], v[62:63] op_sel_hi:[0,1,1]
	v_pk_fma_f32 v[70:71], v[22:23], v[182:183], v[170:171] op_sel_hi:[0,1,1]
	v_pk_fma_f32 v[170:171], v[22:23], v[184:185], v[172:173] op_sel_hi:[0,1,1]
	v_lshl_add_u64 v[172:173], v[68:69], 0, s[8:9]
	v_add_co_u32_e64 v68, s[2:3], s72, v68
	s_mov_b32 s16, 35
	s_nop 0
	v_addc_co_u32_e64 v69, s[2:3], 0, v69, s[2:3]
	v_cvt_f32_fp8_e32 v56, v204
	v_cvt_f32_fp8_sdwa v57, v204 src0_sel:BYTE_1
	v_cvt_f32_fp8_e32 v176, v205
	v_cvt_f32_fp8_sdwa v177, v205 src0_sel:BYTE_1
	v_cvt_f32_fp8_sdwa v178, v205 src0_sel:BYTE_2
	v_cvt_f32_fp8_sdwa v179, v205 src0_sel:BYTE_3
	v_cvt_f32_fp8_e32 v180, v206
	v_cvt_f32_fp8_sdwa v181, v206 src0_sel:BYTE_1
	v_cvt_f32_fp8_sdwa v186, v207 src0_sel:BYTE_2
	v_cvt_f32_fp8_sdwa v187, v207 src0_sel:BYTE_3
	global_load_dword v204, v[68:69], off nt
	global_load_dword v205, v[172:173], off offset:256 nt
	global_load_dword v206, v[172:173], off offset:512 nt
	global_load_dword v207, v[172:173], off offset:768 nt
	s_ashr_i32 s17, s16, 31
	s_lshl_b64 s[2:3], s[16:17], 3
	s_add_u32 s2, s0, s2
	s_addc_u32 s3, s1, s3
	s_load_dwordx2 s[2:3], s[2:3], 0x0
	s_waitcnt vmcnt(27)
	v_cvt_f32_fp8_e32 v68, v169
	v_cvt_f32_fp8_sdwa v69, v169 src0_sel:BYTE_1
	v_pk_fma_f32 v[56:57], v[22:23], v[56:57], v[60:61] op_sel_hi:[0,1,1]
	v_pk_fma_f32 v[60:61], v[22:23], v[178:179], v[114:115] op_sel_hi:[0,1,1]
	v_pk_fma_f32 v[64:65], v[22:23], v[176:177], v[64:65] op_sel_hi:[0,1,1]
	v_pk_fma_f32 v[114:115], v[22:23], v[180:181], v[116:117] op_sel_hi:[0,1,1]
	v_pk_fma_f32 v[116:117], v[22:23], v[186:187], v[174:175] op_sel_hi:[0,1,1]
	v_cvt_f32_fp8_sdwa v172, v169 src0_sel:BYTE_2
	v_cvt_f32_fp8_sdwa v173, v169 src0_sel:BYTE_3
	s_waitcnt vmcnt(26)
	v_cvt_f32_fp8_e32 v174, v208
	v_cvt_f32_fp8_sdwa v175, v208 src0_sel:BYTE_1
	v_cvt_f32_fp8_sdwa v176, v208 src0_sel:BYTE_2
	v_cvt_f32_fp8_sdwa v177, v208 src0_sel:BYTE_3
	s_waitcnt vmcnt(25)
	v_cvt_f32_fp8_e32 v178, v209
	v_cvt_f32_fp8_sdwa v179, v209 src0_sel:BYTE_1
	v_cvt_f32_fp8_sdwa v180, v209 src0_sel:BYTE_2
	v_cvt_f32_fp8_sdwa v181, v209 src0_sel:BYTE_3
	s_waitcnt vmcnt(24)
	v_cvt_f32_fp8_e32 v182, v210
	v_cvt_f32_fp8_sdwa v183, v210 src0_sel:BYTE_1
	v_cvt_f32_fp8_sdwa v184, v210 src0_sel:BYTE_2
	v_cvt_f32_fp8_sdwa v185, v210 src0_sel:BYTE_3
	v_pk_fma_f32 v[186:187], v[22:23], v[68:69], v[56:57] op_sel:[1,0,0]
	s_waitcnt lgkmcnt(0)
	v_lshl_add_u64 v[56:57], s[2:3], 0, v[66:67]
	v_lshl_add_u64 v[56:57], v[56:57], 0, v[74:75]
	v_pk_fma_f32 v[172:173], v[22:23], v[172:173], v[62:63] op_sel:[1,0,0]
	v_pk_fma_f32 v[174:175], v[22:23], v[174:175], v[64:65] op_sel:[1,0,0]
	v_pk_fma_f32 v[176:177], v[22:23], v[176:177], v[60:61] op_sel:[1,0,0]
	v_pk_fma_f32 v[178:179], v[22:23], v[178:179], v[114:115] op_sel:[1,0,0]
	v_pk_fma_f32 v[180:181], v[22:23], v[180:181], v[70:71] op_sel:[1,0,0]
	v_pk_fma_f32 v[170:171], v[22:23], v[182:183], v[170:171] op_sel:[1,0,0]
	v_pk_fma_f32 v[182:183], v[22:23], v[184:185], v[116:117] op_sel:[1,0,0]
	v_mov_b64_e32 v[22:23], v[58:59]
	v_lshl_add_u64 v[58:59], v[56:57], 0, s[8:9]
	v_add_co_u32_e64 v56, s[2:3], s72, v56
	s_mov_b32 s12, 35
	s_nop 0
	v_addc_co_u32_e64 v57, s[2:3], 0, v57, s[2:3]
	global_load_dword v208, v[56:57], off nt
	global_load_dword v209, v[58:59], off offset:256 nt
	global_load_dword v210, v[58:59], off offset:512 nt
	global_load_dword v227, v[58:59], off offset:768 nt
	ds_read_b128 v[68:71], v168
	ds_read_b128 v[64:67], v168 offset:1024
	ds_read_b128 v[60:63], v168 offset:2048
	ds_read_b128 v[56:59], v168 offset:3072
	s_ashr_i32 s13, s12, 31
	s_lshl_b64 s[2:3], s[12:13], 3
	s_waitcnt vmcnt(27)
	v_cvt_f32_fp8_e32 v168, v211
	v_cvt_f32_fp8_sdwa v169, v211 src0_sel:BYTE_1
	s_add_u32 s2, s0, s2
	s_waitcnt vmcnt(26)
	v_cvt_f32_fp8_e32 v188, v212
	v_cvt_f32_fp8_sdwa v189, v212 src0_sel:BYTE_1
	v_cvt_f32_fp8_sdwa v190, v212 src0_sel:BYTE_2
	v_cvt_f32_fp8_sdwa v191, v212 src0_sel:BYTE_3
	s_waitcnt vmcnt(25)
	v_cvt_f32_fp8_e32 v192, v213
	v_cvt_f32_fp8_sdwa v193, v213 src0_sel:BYTE_1
	s_addc_u32 s3, s1, s3
	s_load_dwordx2 s[2:3], s[2:3], 0x0
	v_cvt_f32_fp8_sdwa v194, v213 src0_sel:BYTE_2
	v_cvt_f32_fp8_sdwa v195, v213 src0_sel:BYTE_3
	s_waitcnt lgkmcnt(0)
	v_pk_fma_f32 v[152:153], v[70:71], v[152:153], v[122:123]
	v_pk_fma_f32 v[150:151], v[68:69], v[150:151], v[118:119]
	v_pk_fma_f32 v[164:165], v[66:67], v[164:165], v[126:127]
	v_pk_fma_f32 v[154:155], v[64:65], v[154:155], v[120:121]
	v_pk_fma_f32 v[130:131], v[62:63], v[156:157], v[130:131]
	v_pk_fma_f32 v[156:157], v[60:61], v[158:159], v[124:125]
	v_pk_fma_f32 v[158:159], v[56:57], v[162:163], v[128:129]
	v_pk_fma_f32 v[120:121], v[70:71], v[172:173], v[138:139]
	v_pk_fma_f32 v[128:129], v[68:69], v[186:187], v[132:133]
	v_pk_fma_f32 v[114:115], v[66:67], v[176:177], v[142:143]
	v_pk_fma_f32 v[122:123], v[64:65], v[174:175], v[136:137]
	v_pk_fma_f32 v[134:135], v[58:59], v[160:161], v[134:135]
	v_pk_fma_f32 v[116:117], v[62:63], v[180:181], v[146:147]
	v_pk_fma_f32 v[124:125], v[60:61], v[178:179], v[140:141]
	v_pk_fma_f32 v[118:119], v[58:59], v[182:183], v[148:149]
	v_pk_fma_f32 v[126:127], v[56:57], v[170:171], v[144:145]
	v_pk_fma_f32 v[136:137], v[24:25], v[168:169], 0 op_sel_hi:[0,1,0]
	v_pk_mul_f32 v[160:161], v[150:151], v[150:151]
	v_pk_mul_f32 v[162:163], v[152:153], v[152:153]
	v_pk_mul_f32 v[168:169], v[154:155], v[154:155]
	v_pk_mul_f32 v[170:171], v[164:165], v[164:165]
	v_mul_f32_e32 v172, v157, v157
	v_mul_f32_e32 v174, v131, v131
	v_pk_mul_f32 v[176:177], v[128:129], v[128:129]
	v_pk_mul_f32 v[178:179], v[120:121], v[120:121]
	v_pk_mul_f32 v[180:181], v[122:123], v[122:123]
	v_pk_mul_f32 v[182:183], v[114:115], v[114:115]
	v_pk_fma_f32 v[138:139], v[24:25], v[190:191], 0 op_sel_hi:[0,1,0]
	v_pk_fma_f32 v[140:141], v[24:25], v[188:189], 0 op_sel_hi:[0,1,0]
	v_pk_fma_f32 v[144:145], v[24:25], v[192:193], 0 op_sel_hi:[0,1,0]
	v_mul_f32_e32 v191, v134, v134
	v_mul_f32_e32 v192, v135, v135
	v_pk_mov_b32 v[188:189], v[160:161], v[162:163] op_sel:[1,0]
	v_mov_b32_e32 v161, v163
	v_pk_mov_b32 v[162:163], v[168:169], v[170:171] op_sel:[1,0]
	v_mov_b32_e32 v169, v171
	v_pk_fma_f32 v[170:171], v[156:157], v[156:157], v[172:173] op_sel_hi:[1,1,0]
	v_pk_fma_f32 v[172:173], v[130:131], v[130:131], v[174:175] op_sel_hi:[1,1,0]
	v_pk_mov_b32 v[174:175], v[176:177], v[178:179] op_sel:[1,0]
	v_mov_b32_e32 v177, v179
	v_pk_mov_b32 v[178:179], v[180:181], v[182:183] op_sel:[1,0]
	v_mov_b32_e32 v181, v183
	v_pk_add_f32 v[160:161], v[188:189], v[160:161]
	v_pk_add_f32 v[162:163], v[162:163], v[168:169]
	v_mov_b32_e32 v171, v191
	v_mov_b32_e32 v173, v192
	v_pk_add_f32 v[168:169], v[174:175], v[176:177]
	v_pk_add_f32 v[174:175], v[178:179], v[180:181]
	v_pk_fma_f32 v[142:143], v[24:25], v[194:195], 0 op_sel_hi:[0,1,0]
	v_mul_f32_e32 v187, v158, v158
	v_mul_f32_e32 v190, v159, v159
	v_mul_f32_e32 v193, v126, v126
	v_mul_f32_e32 v194, v127, v127
	v_pk_add_f32 v[160:161], v[160:161], v[160:161] op_sel:[0,1] op_sel_hi:[1,0]
	v_pk_add_f32 v[162:163], v[162:163], v[162:163] op_sel:[0,1] op_sel_hi:[1,0]
	v_pk_add_f32 v[170:171], v[170:171], v[172:173]
	v_pk_add_f32 v[168:169], v[168:169], v[168:169] op_sel:[0,1] op_sel_hi:[1,0]
	v_pk_add_f32 v[172:173], v[174:175], v[174:175] op_sel:[0,1] op_sel_hi:[1,0]
	v_lshl_add_u64 v[96:97], s[2:3], 0, v[96:97]
	v_mov_b32_e32 v161, v187
	v_mov_b32_e32 v163, v190
	v_mov_b32_e32 v169, v193
	v_mov_b32_e32 v173, v194
	v_lshl_add_u64 v[96:97], v[96:97], 0, v[74:75]
	v_pk_add_f32 v[160:161], v[160:161], v[162:163]
	v_pk_add_f32 v[162:163], v[168:169], v[172:173]
	v_lshl_add_u64 v[168:169], v[96:97], 0, s[8:9]
	v_add_co_u32_e64 v96, s[2:3], s72, v96
	v_cvt_f32_fp8_sdwa v184, v211 src0_sel:BYTE_2
	s_nop 0
	v_addc_co_u32_e64 v97, s[2:3], 0, v97, s[2:3]
	global_load_dword v178, v[96:97], off nt
	global_load_dword v179, v[168:169], off offset:256 nt
	global_load_dword v180, v[168:169], off offset:512 nt
	global_load_dword v181, v[168:169], off offset:768 nt
	v_cvt_f32_fp8_sdwa v185, v211 src0_sel:BYTE_3
	s_waitcnt vmcnt(28)
	v_cvt_f32_fp8_e32 v196, v214
	v_cvt_f32_fp8_sdwa v197, v214 src0_sel:BYTE_1
	v_pk_add_f32 v[160:161], v[160:161], v[170:171]
	v_pk_fma_f32 v[132:133], v[24:25], v[184:185], 0 op_sel_hi:[0,1,0]
	v_mul_f32_e32 v184, v125, v125
	v_mul_f32_e32 v186, v117, v117
	v_add_f32_e32 v74, v160, v161
	v_pk_fma_f32 v[148:149], v[24:25], v[196:197], 0 op_sel_hi:[0,1,0]
	v_mul_f32_e32 v195, v118, v118
	v_mul_f32_e32 v196, v119, v119
	v_pk_fma_f32 v[182:183], v[124:125], v[124:125], v[184:185] op_sel_hi:[1,1,0]
	v_pk_fma_f32 v[184:185], v[116:117], v[116:117], v[186:187] op_sel_hi:[1,1,0]
	v_add_f32_dpp v74, v74, v74 quad_perm:[1,0,3,2] row_mask:0xf bank_mask:0xf bound_ctrl:1
	v_mov_b32_e32 v183, v195
	v_mov_b32_e32 v185, v196
	v_add_f32_dpp v74, v74, v74 quad_perm:[2,3,0,1] row_mask:0xf bank_mask:0xf bound_ctrl:1
	v_pk_add_f32 v[174:175], v[182:183], v[184:185]
	v_mbcnt_lo_u32_b32 v96, -1, 0
	v_mbcnt_hi_u32_b32 v96, -1, v96
	v_cvt_f32_fp8_sdwa v198, v214 src0_sel:BYTE_2
	v_lshlrev_b32_e32 v182, 2, v96
	v_add_f32_dpp v74, v74, v74 row_half_mirror row_mask:0xf bank_mask:0xf bound_ctrl:1
	v_pk_add_f32 v[162:163], v[162:163], v[174:175]
	v_xor_b32_e32 v182, 64, v182
	v_add_f32_dpp v74, v74, v74 row_mirror row_mask:0xf bank_mask:0xf bound_ctrl:1
	v_cvt_f32_fp8_sdwa v199, v214 src0_sel:BYTE_3
	v_add_f32_e32 v97, v162, v163
	ds_bpermute_b32 v182, v182, v74
	s_waitcnt vmcnt(27)
	v_cvt_f32_fp8_e32 v96, v215
	v_add_f32_dpp v183, v97, v97 quad_perm:[1,0,3,2] row_mask:0xf bank_mask:0xf bound_ctrl:1
	v_cvt_f32_fp8_sdwa v97, v215 src0_sel:BYTE_1
	v_cvt_f32_fp8_sdwa v160, v215 src0_sel:BYTE_2
	v_cvt_f32_fp8_sdwa v161, v215 src0_sel:BYTE_3
	s_waitcnt vmcnt(26)
	v_cvt_f32_fp8_e32 v162, v216
	v_cvt_f32_fp8_sdwa v163, v216 src0_sel:BYTE_1
	v_cvt_f32_fp8_sdwa v168, v216 src0_sel:BYTE_2
	v_cvt_f32_fp8_sdwa v169, v216 src0_sel:BYTE_3
	s_waitcnt vmcnt(25)
	v_cvt_f32_fp8_e32 v170, v217
	v_cvt_f32_fp8_sdwa v171, v217 src0_sel:BYTE_1
	v_cvt_f32_fp8_sdwa v172, v217 src0_sel:BYTE_2
	v_cvt_f32_fp8_sdwa v173, v217 src0_sel:BYTE_3
	s_waitcnt vmcnt(24)
	v_cvt_f32_fp8_e32 v174, v218
	v_cvt_f32_fp8_sdwa v175, v218 src0_sel:BYTE_1
	v_cvt_f32_fp8_sdwa v176, v218 src0_sel:BYTE_2
	v_cvt_f32_fp8_sdwa v177, v218 src0_sel:BYTE_3
	v_pk_fma_f32 v[146:147], v[24:25], v[198:199], 0 op_sel_hi:[0,1,0]
	v_pk_fma_f32 v[96:97], v[24:25], v[96:97], v[136:137] op_sel:[1,0,0]
	v_pk_fma_f32 v[132:133], v[24:25], v[160:161], v[132:133] op_sel:[1,0,0]
	v_pk_fma_f32 v[136:137], v[24:25], v[162:163], v[140:141] op_sel:[1,0,0]
	v_pk_fma_f32 v[138:139], v[24:25], v[168:169], v[138:139] op_sel:[1,0,0]
	v_pk_fma_f32 v[140:141], v[24:25], v[170:171], v[144:145] op_sel:[1,0,0]
	v_pk_fma_f32 v[142:143], v[24:25], v[172:173], v[142:143] op_sel:[1,0,0]
	v_pk_fma_f32 v[144:145], v[24:25], v[174:175], v[148:149] op_sel:[1,0,0]
	v_pk_fma_f32 v[146:147], v[24:25], v[176:177], v[146:147] op_sel:[1,0,0]
	v_mov_b64_e32 v[24:25], v[52:53]
	s_waitcnt lgkmcnt(0)
	v_add_f32_e32 v52, v74, v182
	v_mov_b32_e32 v53, v52
	s_mov_b32 s66, 34
	s_nop 1
	v_permlane32_swap_b32 v52, v53
	s_ashr_i32 s67, s66, 31
	v_add_f32_e32 v52, v52, v53
	v_fmamk_f32 v74, v52, 0x3a800000, v73
	s_lshl_b64 s[10:11], s[66:67], 3
	v_mul_f32_e32 v176, 0x4b800000, v74
	s_add_u32 s10, s0, s10
	v_cmp_gt_f32_e64 s[2:3], s74, v74
	s_addc_u32 s11, s1, s11
	s_waitcnt vmcnt(23)
	v_cvt_f32_fp8_sdwa v148, v219 src0_sel:BYTE_2
	v_cndmask_b32_e64 v74, v74, v176, s[2:3]
	v_cvt_f32_fp8_sdwa v149, v219 src0_sel:BYTE_3
	v_rsq_f32_e32 v74, v74
	s_load_dwordx2 s[10:11], s[10:11], 0x0
	v_cvt_f32_fp8_e32 v52, v219
	v_cvt_f32_fp8_sdwa v53, v219 src0_sel:BYTE_1
	s_waitcnt vmcnt(22)
	v_cvt_f32_fp8_e32 v160, v220
	v_cvt_f32_fp8_sdwa v161, v220 src0_sel:BYTE_1
	v_cvt_f32_fp8_sdwa v162, v220 src0_sel:BYTE_2
	v_cvt_f32_fp8_sdwa v163, v220 src0_sel:BYTE_3
	s_waitcnt vmcnt(21)
	v_cvt_f32_fp8_e32 v168, v221
	v_cvt_f32_fp8_sdwa v169, v221 src0_sel:BYTE_1
	v_cvt_f32_fp8_sdwa v170, v221 src0_sel:BYTE_2
	v_cvt_f32_fp8_sdwa v171, v221 src0_sel:BYTE_3
	s_waitcnt vmcnt(20)
	v_cvt_f32_fp8_e32 v172, v222
	v_cvt_f32_fp8_sdwa v173, v222 src0_sel:BYTE_1
	v_pk_fma_f32 v[148:149], v[26:27], v[148:149], v[132:133] op_sel_hi:[0,1,1]
	v_mul_f32_e32 v132, 0x45800000, v74
	v_cndmask_b32_e64 v74, v74, v132, s[2:3]
	s_waitcnt lgkmcnt(0)
	v_lshl_add_u64 v[132:133], s[10:11], 0, v[78:79]
	v_pk_fma_f32 v[52:53], v[26:27], v[52:53], v[96:97] op_sel_hi:[0,1,1]
	v_pk_fma_f32 v[96:97], v[26:27], v[162:163], v[138:139] op_sel_hi:[0,1,1]
	v_pk_fma_f32 v[160:161], v[26:27], v[160:161], v[136:137] op_sel_hi:[0,1,1]
	v_pk_mul_f32 v[136:137], v[150:151], v[74:75] op_sel_hi:[1,0]
	v_pk_mul_f32 v[138:139], v[152:153], v[74:75] op_sel_hi:[1,0]
	v_add_co_u32_e64 v150, s[2:3], s75, v132
	v_pk_fma_f32 v[162:163], v[26:27], v[170:171], v[142:143] op_sel_hi:[0,1,1]
	v_pk_fma_f32 v[168:169], v[26:27], v[168:169], v[140:141] op_sel_hi:[0,1,1]
	v_pk_fma_f32 v[170:171], v[26:27], v[172:173], v[144:145] op_sel_hi:[0,1,1]
	v_addc_co_u32_e64 v151, s[2:3], -1, v133, s[2:3]
	v_pk_mul_f32 v[140:141], v[154:155], v[74:75] op_sel_hi:[1,0]
	v_pk_mul_f32 v[142:143], v[164:165], v[74:75] op_sel_hi:[1,0]
	v_pk_mul_f32 v[144:145], v[156:157], v[74:75] op_sel_hi:[1,0]
	v_pk_mul_f32 v[152:153], v[130:131], v[74:75] op_sel_hi:[1,0]
	v_pk_mul_f32 v[154:155], v[158:159], v[74:75] op_sel_hi:[1,0]
	v_pk_mul_f32 v[156:157], v[134:135], v[74:75] op_sel_hi:[1,0]
	v_pk_mul_f32 v[132:133], v[2:3], v[138:139]
	v_pk_mul_f32 v[130:131], v[0:1], v[136:137]
	v_add_f32_dpp v183, v183, v183 quad_perm:[2,3,0,1] row_mask:0xf bank_mask:0xf bound_ctrl:1
	v_pk_mul_f32 v[136:137], v[6:7], v[142:143]
	v_pk_mul_f32 v[134:135], v[4:5], v[140:141]
	v_pk_mul_f32 v[140:141], v[10:11], v[152:153]
	v_pk_mul_f32 v[138:139], v[8:9], v[144:145]
	v_pk_mul_f32 v[144:145], v[14:15], v[156:157]
	v_pk_mul_f32 v[142:143], v[12:13], v[154:155]
	global_store_dwordx4 v[150:151], v[130:133], off offset:-3072 nt
	global_store_dwordx4 v[150:151], v[134:137], off offset:-2048 nt
	global_store_dwordx4 v[150:151], v[138:141], off offset:-1024 nt
	global_store_dwordx4 v[150:151], v[142:145], off nt
	v_mbcnt_lo_u32_b32 v74, -1, 0
	v_mbcnt_hi_u32_b32 v74, -1, v74
	v_add_f32_dpp v183, v183, v183 row_half_mirror row_mask:0xf bank_mask:0xf bound_ctrl:1
	v_lshlrev_b32_e32 v74, 2, v74
	v_xor_b32_e32 v74, 64, v74
	v_add_f32_dpp v183, v183, v183 row_mirror row_mask:0xf bank_mask:0xf bound_ctrl:1
	v_cvt_f32_fp8_sdwa v174, v222 src0_sel:BYTE_2
	v_cvt_f32_fp8_sdwa v175, v222 src0_sel:BYTE_3
	s_waitcnt vmcnt(23)
	v_cvt_f32_fp8_e32 v130, v223
	v_cvt_f32_fp8_sdwa v131, v223 src0_sel:BYTE_1
	v_cvt_f32_fp8_sdwa v132, v223 src0_sel:BYTE_2
	v_cvt_f32_fp8_sdwa v133, v223 src0_sel:BYTE_3
	s_waitcnt vmcnt(22)
	v_cvt_f32_fp8_e32 v134, v224
	v_cvt_f32_fp8_sdwa v135, v224 src0_sel:BYTE_1
	v_cvt_f32_fp8_sdwa v136, v224 src0_sel:BYTE_2
	v_cvt_f32_fp8_sdwa v137, v224 src0_sel:BYTE_3
	s_waitcnt vmcnt(21)
	v_cvt_f32_fp8_e32 v138, v225
	v_cvt_f32_fp8_sdwa v139, v225 src0_sel:BYTE_1
	v_cvt_f32_fp8_sdwa v140, v225 src0_sel:BYTE_2
	v_cvt_f32_fp8_sdwa v141, v225 src0_sel:BYTE_3
	ds_bpermute_b32 v74, v74, v183
	s_waitcnt vmcnt(20)
	v_cvt_f32_fp8_e32 v142, v226
	v_cvt_f32_fp8_sdwa v143, v226 src0_sel:BYTE_1
	v_cvt_f32_fp8_sdwa v144, v226 src0_sel:BYTE_2
	v_cvt_f32_fp8_sdwa v145, v226 src0_sel:BYTE_3
	v_lshlrev_b32_e32 v98, 16, v100
	v_and_b32_e32 v99, 0xffff0000, v100
	v_lshlrev_b32_e32 v102, 16, v101
	v_and_b32_e32 v103, 0xffff0000, v101
	v_lshlrev_b32_e32 v100, 16, v104
	v_and_b32_e32 v101, 0xffff0000, v104
	v_lshlrev_b32_e32 v106, 16, v105
	v_and_b32_e32 v107, 0xffff0000, v105
	v_lshlrev_b32_e32 v104, 16, v108
	v_and_b32_e32 v105, 0xffff0000, v108
	v_lshlrev_b32_e32 v110, 16, v109
	v_and_b32_e32 v111, 0xffff0000, v109
	v_pk_fma_f32 v[146:147], v[26:27], v[174:175], v[146:147] op_sel_hi:[0,1,1]
	v_pk_fma_f32 v[52:53], v[26:27], v[130:131], v[52:53] op_sel:[1,0,0]
	v_pk_fma_f32 v[130:131], v[26:27], v[132:133], v[148:149] op_sel:[1,0,0]
	v_pk_fma_f32 v[132:133], v[26:27], v[134:135], v[160:161] op_sel:[1,0,0]
	v_pk_fma_f32 v[96:97], v[26:27], v[136:137], v[96:97] op_sel:[1,0,0]
	v_pk_fma_f32 v[134:135], v[26:27], v[138:139], v[168:169] op_sel:[1,0,0]
	v_pk_fma_f32 v[136:137], v[26:27], v[140:141], v[162:163] op_sel:[1,0,0]
	v_lshlrev_b32_e32 v108, 16, v112
	v_and_b32_e32 v109, 0xffff0000, v112
	v_lshlrev_b32_e32 v112, 16, v113
	v_and_b32_e32 v113, 0xffff0000, v113
	v_pk_fma_f32 v[138:139], v[26:27], v[142:143], v[170:171] op_sel:[1,0,0]
	v_pk_fma_f32 v[140:141], v[26:27], v[144:145], v[146:147] op_sel:[1,0,0]
	v_pk_fma_f32 v[130:131], v[70:71], v[130:131], v[102:103]
	v_pk_fma_f32 v[142:143], v[68:69], v[52:53], v[98:99]
	v_pk_fma_f32 v[144:145], v[66:67], v[96:97], v[106:107]
	v_pk_fma_f32 v[132:133], v[64:65], v[132:133], v[100:101]
	v_pk_fma_f32 v[110:111], v[62:63], v[136:137], v[110:111]
	v_pk_fma_f32 v[134:135], v[60:61], v[134:135], v[104:105]
	s_waitcnt lgkmcnt(0)
	v_add_f32_e32 v104, v183, v74
	s_mov_b32 s64, 34
	v_mov_b64_e32 v[26:27], v[54:55]
	v_pk_fma_f32 v[112:113], v[58:59], v[140:141], v[112:113]
	v_mov_b32_e32 v105, v104
	v_pk_mul_f32 v[52:53], v[142:143], v[142:143]
	v_pk_mul_f32 v[54:55], v[130:131], v[130:131]
	v_pk_mul_f32 v[96:97], v[132:133], v[132:133]
	v_pk_mul_f32 v[98:99], v[144:145], v[144:145]
	v_mul_f32_e32 v74, v135, v135
	v_mul_f32_e32 v100, v111, v111
	v_mul_f32_e32 v136, v112, v112
	v_mul_f32_e32 v137, v113, v113
	s_nop 1
	v_permlane32_swap_b32 v104, v105
	v_pk_mov_b32 v[102:103], v[52:53], v[54:55] op_sel:[1,0]
	v_mov_b32_e32 v53, v55
	v_pk_mov_b32 v[54:55], v[96:97], v[98:99] op_sel:[1,0]
	v_mov_b32_e32 v97, v99
	v_pk_fma_f32 v[98:99], v[134:135], v[134:135], v[74:75] op_sel_hi:[1,1,0]
	v_pk_fma_f32 v[100:101], v[110:111], v[110:111], v[100:101] op_sel_hi:[1,1,0]
	v_add_f32_e32 v74, v104, v105
	s_ashr_i32 s65, s64, 31
	v_pk_fma_f32 v[108:109], v[56:57], v[138:139], v[108:109]
	v_pk_add_f32 v[52:53], v[102:103], v[52:53]
	v_pk_add_f32 v[54:55], v[54:55], v[96:97]
	v_mov_b32_e32 v99, v136
	v_mov_b32_e32 v101, v137
	v_fmamk_f32 v74, v74, 0x3a800000, v73
	s_lshl_b64 s[10:11], s[64:65], 3
	v_mul_f32_e32 v106, v108, v108
	v_mul_f32_e32 v107, v109, v109
	v_pk_add_f32 v[52:53], v[52:53], v[52:53] op_sel:[0,1] op_sel_hi:[1,0]
	v_pk_add_f32 v[54:55], v[54:55], v[54:55] op_sel:[0,1] op_sel_hi:[1,0]
	v_pk_add_f32 v[96:97], v[98:99], v[100:101]
	v_mul_f32_e32 v98, 0x4b800000, v74
	s_add_u32 s10, s0, s10
	v_cmp_gt_f32_e64 s[2:3], s74, v74
	v_mov_b32_e32 v53, v106
	v_mov_b32_e32 v55, v107
	v_cndmask_b32_e64 v74, v74, v98, s[2:3]
	s_addc_u32 s11, s1, s11
	v_pk_add_f32 v[52:53], v[52:53], v[54:55]
	v_rsq_f32_e32 v74, v74
	s_load_dwordx2 s[10:11], s[10:11], 0x0
	v_pk_add_f32 v[52:53], v[52:53], v[96:97]
	s_waitcnt vmcnt(19)
	v_cvt_f32_fp8_e32 v54, v200
	v_cvt_f32_fp8_sdwa v55, v200 src0_sel:BYTE_1
	v_cvt_f32_fp8_sdwa v96, v200 src0_sel:BYTE_2
	v_cvt_f32_fp8_sdwa v97, v200 src0_sel:BYTE_3
	s_waitcnt vmcnt(18)
	v_cvt_f32_fp8_e32 v98, v201
	v_cvt_f32_fp8_sdwa v99, v201 src0_sel:BYTE_1
	v_add_f32_e32 v52, v52, v53
	v_cvt_f32_fp8_sdwa v100, v201 src0_sel:BYTE_2
	v_cvt_f32_fp8_sdwa v101, v201 src0_sel:BYTE_3
	s_waitcnt vmcnt(17)
	v_cvt_f32_fp8_e32 v102, v202
	v_cvt_f32_fp8_sdwa v103, v202 src0_sel:BYTE_1
	v_cvt_f32_fp8_sdwa v104, v202 src0_sel:BYTE_2
	v_cvt_f32_fp8_sdwa v105, v202 src0_sel:BYTE_3
	s_waitcnt vmcnt(16)
	v_cvt_f32_fp8_e32 v106, v203
	v_cvt_f32_fp8_sdwa v107, v203 src0_sel:BYTE_1
	v_add_f32_dpp v52, v52, v52 quad_perm:[1,0,3,2] row_mask:0xf bank_mask:0xf bound_ctrl:1
	v_mul_f32_e32 v53, 0x45800000, v74
	v_pk_fma_f32 v[138:139], v[28:29], v[54:55], 0 op_sel_hi:[0,1,0]
	v_add_f32_dpp v52, v52, v52 quad_perm:[2,3,0,1] row_mask:0xf bank_mask:0xf bound_ctrl:1
	s_waitcnt lgkmcnt(0)
	v_lshl_add_u64 v[54:55], s[10:11], 0, v[78:79]
	v_pk_fma_f32 v[140:141], v[28:29], v[96:97], 0 op_sel_hi:[0,1,0]
	v_add_f32_dpp v156, v52, v52 row_half_mirror row_mask:0xf bank_mask:0xf bound_ctrl:1
	v_cndmask_b32_e64 v52, v74, v53, s[2:3]
	v_pk_fma_f32 v[146:147], v[28:29], v[98:99], 0 op_sel_hi:[0,1,0]
	v_pk_mul_f32 v[96:97], v[128:129], v[52:53] op_sel_hi:[1,0]
	v_pk_mul_f32 v[98:99], v[120:121], v[52:53] op_sel_hi:[1,0]
	v_add_co_u32_e64 v120, s[2:3], s76, v54
	v_pk_fma_f32 v[148:149], v[28:29], v[100:101], 0 op_sel_hi:[0,1,0]
	v_pk_fma_f32 v[150:151], v[28:29], v[104:105], 0 op_sel_hi:[0,1,0]
	v_pk_fma_f32 v[152:153], v[28:29], v[102:103], 0 op_sel_hi:[0,1,0]
	v_pk_fma_f32 v[154:155], v[28:29], v[106:107], 0 op_sel_hi:[0,1,0]
	v_addc_co_u32_e64 v121, s[2:3], -1, v55, s[2:3]
	v_pk_mul_f32 v[100:101], v[122:123], v[52:53] op_sel_hi:[1,0]
	v_pk_mul_f32 v[102:103], v[114:115], v[52:53] op_sel_hi:[1,0]
	v_pk_mul_f32 v[104:105], v[124:125], v[52:53] op_sel_hi:[1,0]
	v_pk_mul_f32 v[106:107], v[116:117], v[52:53] op_sel_hi:[1,0]
	v_pk_mul_f32 v[114:115], v[126:127], v[52:53] op_sel_hi:[1,0]
	v_pk_mul_f32 v[116:117], v[118:119], v[52:53] op_sel_hi:[1,0]
	v_pk_mul_f32 v[54:55], v[2:3], v[98:99]
	v_pk_mul_f32 v[52:53], v[0:1], v[96:97]
	v_pk_mul_f32 v[98:99], v[6:7], v[102:103]
	v_pk_mul_f32 v[96:97], v[4:5], v[100:101]
	v_pk_mul_f32 v[102:103], v[10:11], v[106:107]
	v_pk_mul_f32 v[100:101], v[8:9], v[104:105]
	v_pk_mul_f32 v[106:107], v[14:15], v[116:117]
	v_pk_mul_f32 v[104:105], v[12:13], v[114:115]
	global_store_dwordx4 v[120:121], v[52:55], off offset:-3072 nt
	global_store_dwordx4 v[120:121], v[96:99], off offset:-2048 nt
	global_store_dwordx4 v[120:121], v[100:103], off offset:-1024 nt
	global_store_dwordx4 v[120:121], v[104:107], off nt
	v_mbcnt_lo_u32_b32 v52, -1, 0
	v_mbcnt_hi_u32_b32 v52, -1, v52
	v_add_f32_dpp v74, v156, v156 row_mirror row_mask:0xf bank_mask:0xf bound_ctrl:1
	v_lshlrev_b32_e32 v52, 2, v52
	v_xor_b32_e32 v52, 64, v52
	ds_bpermute_b32 v114, v52, v74
	v_cvt_f32_fp8_sdwa v136, v203 src0_sel:BYTE_2
	v_cvt_f32_fp8_sdwa v137, v203 src0_sel:BYTE_3
	s_waitcnt vmcnt(19)
	v_cvt_f32_fp8_e32 v52, v204
	v_cvt_f32_fp8_sdwa v53, v204 src0_sel:BYTE_1
	v_cvt_f32_fp8_sdwa v54, v204 src0_sel:BYTE_2
	v_cvt_f32_fp8_sdwa v55, v204 src0_sel:BYTE_3
	s_waitcnt vmcnt(18)
	v_cvt_f32_fp8_e32 v96, v205
	v_cvt_f32_fp8_sdwa v97, v205 src0_sel:BYTE_1
	v_cvt_f32_fp8_sdwa v98, v205 src0_sel:BYTE_2
	v_cvt_f32_fp8_sdwa v99, v205 src0_sel:BYTE_3
	s_waitcnt vmcnt(17)
	v_cvt_f32_fp8_e32 v100, v206
	v_cvt_f32_fp8_sdwa v101, v206 src0_sel:BYTE_1
	v_cvt_f32_fp8_sdwa v102, v206 src0_sel:BYTE_2
	v_cvt_f32_fp8_sdwa v103, v206 src0_sel:BYTE_3
	s_waitcnt vmcnt(16)
	v_cvt_f32_fp8_e32 v104, v207
	v_cvt_f32_fp8_sdwa v105, v207 src0_sel:BYTE_1
	v_cvt_f32_fp8_sdwa v106, v207 src0_sel:BYTE_2
	v_cvt_f32_fp8_sdwa v107, v207 src0_sel:BYTE_3
	s_waitcnt lgkmcnt(0)
	v_add_f32_e32 v74, v74, v114
	s_mov_b32 s68, 34
	v_pk_fma_f32 v[136:137], v[28:29], v[136:137], 0 op_sel_hi:[0,1,0]
	v_mov_b32_e32 v156, v74
	v_pk_fma_f32 v[114:115], v[28:29], v[54:55], v[140:141] op_sel:[1,0,0]
	v_pk_fma_f32 v[116:117], v[28:29], v[52:53], v[138:139] op_sel:[1,0,0]
	v_pk_fma_f32 v[118:119], v[28:29], v[98:99], v[148:149] op_sel:[1,0,0]
	v_pk_fma_f32 v[120:121], v[28:29], v[96:97], v[146:147] op_sel:[1,0,0]
	v_pk_fma_f32 v[122:123], v[28:29], v[100:101], v[152:153] op_sel:[1,0,0]
	v_pk_fma_f32 v[124:125], v[28:29], v[102:103], v[150:151] op_sel:[1,0,0]
	v_pk_fma_f32 v[126:127], v[28:29], v[104:105], v[154:155] op_sel:[1,0,0]
	v_pk_fma_f32 v[128:129], v[28:29], v[106:107], v[136:137] op_sel:[1,0,0]
	s_nop 1
	v_permlane32_swap_b32 v74, v156
	v_mov_b64_e32 v[28:29], v[48:49]
	v_add_f32_e32 v48, v74, v156
	s_ashr_i32 s69, s68, 31
	v_fmamk_f32 v48, v48, 0x3a800000, v73
	s_lshl_b64 s[10:11], s[68:69], 3
	v_mul_f32_e32 v49, 0x4b800000, v48
	s_add_u32 s10, s0, s10
	v_cmp_gt_f32_e64 s[2:3], s74, v48
	s_addc_u32 s11, s1, s11
	s_load_dwordx2 s[10:11], s[10:11], 0x0
	v_cndmask_b32_e64 v48, v48, v49, s[2:3]
	v_rsq_f32_e32 v52, v48
	s_waitcnt vmcnt(15)
	v_cvt_f32_fp8_e32 v48, v208
	v_cvt_f32_fp8_sdwa v49, v208 src0_sel:BYTE_1
	s_waitcnt lgkmcnt(0)
	v_lshl_add_u64 v[154:155], s[10:11], 0, v[78:79]
	v_mul_f32_e32 v53, 0x45800000, v52
	v_cndmask_b32_e64 v52, v52, v53, s[2:3]
	s_waitcnt vmcnt(13)
	v_cvt_f32_fp8_e32 v146, v210
	v_cvt_f32_fp8_sdwa v147, v210 src0_sel:BYTE_1
	v_pk_mul_f32 v[96:97], v[142:143], v[52:53] op_sel_hi:[1,0]
	v_pk_mul_f32 v[54:55], v[130:131], v[52:53] op_sel_hi:[1,0]
	v_add_co_u32_e64 v130, s[2:3], s73, v154
	v_pk_mul_f32 v[100:101], v[132:133], v[52:53] op_sel_hi:[1,0]
	s_nop 0
	v_addc_co_u32_e64 v131, s[2:3], -1, v155, s[2:3]
	v_pk_mul_f32 v[98:99], v[144:145], v[52:53] op_sel_hi:[1,0]
	v_pk_mul_f32 v[104:105], v[134:135], v[52:53] op_sel_hi:[1,0]
	v_pk_mul_f32 v[102:103], v[110:111], v[52:53] op_sel_hi:[1,0]
	v_pk_mul_f32 v[108:109], v[108:109], v[52:53] op_sel_hi:[1,0]
	v_pk_mul_f32 v[106:107], v[112:113], v[52:53] op_sel_hi:[1,0]
	v_pk_mul_f32 v[54:55], v[2:3], v[54:55]
	v_pk_mul_f32 v[52:53], v[0:1], v[96:97]
	v_pk_mul_f32 v[98:99], v[6:7], v[98:99]
	v_pk_mul_f32 v[96:97], v[4:5], v[100:101]
	v_pk_mul_f32 v[102:103], v[10:11], v[102:103]
	v_pk_mul_f32 v[100:101], v[8:9], v[104:105]
	v_pk_mul_f32 v[106:107], v[14:15], v[106:107]
	v_pk_mul_f32 v[104:105], v[12:13], v[108:109]
	global_store_dwordx4 v[130:131], v[52:55], off offset:-3072 nt
	global_store_dwordx4 v[130:131], v[96:99], off offset:-2048 nt
	global_store_dwordx4 v[130:131], v[100:103], off offset:-1024 nt
	global_store_dwordx4 v[154:155], v[104:107], off offset:-4096 nt
	v_mbcnt_lo_u32_b32 v52, -1, 0
	v_mbcnt_hi_u32_b32 v52, -1, v52
	v_cvt_f32_fp8_sdwa v136, v208 src0_sel:BYTE_2
	v_cvt_f32_fp8_sdwa v137, v208 src0_sel:BYTE_3
	v_cvt_f32_fp8_e32 v138, v209
	v_cvt_f32_fp8_sdwa v139, v209 src0_sel:BYTE_1
	v_cvt_f32_fp8_sdwa v140, v209 src0_sel:BYTE_2
	v_cvt_f32_fp8_sdwa v141, v209 src0_sel:BYTE_3
	v_lshlrev_b32_e32 v52, 2, v52
	v_cvt_f32_fp8_sdwa v148, v210 src0_sel:BYTE_2
	v_cvt_f32_fp8_sdwa v149, v210 src0_sel:BYTE_3
	s_waitcnt vmcnt(16)
	v_cvt_f32_fp8_e32 v150, v227
	v_cvt_f32_fp8_sdwa v151, v227 src0_sel:BYTE_1
	v_cvt_f32_fp8_sdwa v152, v227 src0_sel:BYTE_2
	v_cvt_f32_fp8_sdwa v153, v227 src0_sel:BYTE_3
	v_pk_fma_f32 v[48:49], v[30:31], v[48:49], v[116:117] op_sel_hi:[0,1,1]
	v_pk_fma_f32 v[116:117], v[30:31], v[146:147], v[122:123] op_sel_hi:[0,1,1]
	v_xor_b32_e32 v122, 64, v52
	s_waitcnt vmcnt(15)
	v_cvt_f32_fp8_e32 v52, v178
	v_cvt_f32_fp8_sdwa v53, v178 src0_sel:BYTE_1
	v_cvt_f32_fp8_sdwa v54, v178 src0_sel:BYTE_2
	v_cvt_f32_fp8_sdwa v55, v178 src0_sel:BYTE_3
	s_waitcnt vmcnt(14)
	v_cvt_f32_fp8_e32 v96, v179
	v_cvt_f32_fp8_sdwa v97, v179 src0_sel:BYTE_1
	v_cvt_f32_fp8_sdwa v98, v179 src0_sel:BYTE_2
	v_cvt_f32_fp8_sdwa v99, v179 src0_sel:BYTE_3
	s_waitcnt vmcnt(13)
	v_cvt_f32_fp8_e32 v100, v180
	v_cvt_f32_fp8_sdwa v101, v180 src0_sel:BYTE_1
	v_cvt_f32_fp8_sdwa v102, v180 src0_sel:BYTE_2
	v_cvt_f32_fp8_sdwa v103, v180 src0_sel:BYTE_3
	s_waitcnt vmcnt(12)
	v_cvt_f32_fp8_e32 v104, v181
	v_cvt_f32_fp8_sdwa v105, v181 src0_sel:BYTE_1
	v_cvt_f32_fp8_sdwa v106, v181 src0_sel:BYTE_2
	v_cvt_f32_fp8_sdwa v107, v181 src0_sel:BYTE_3
	v_pk_fma_f32 v[108:109], v[30:31], v[136:137], v[114:115] op_sel_hi:[0,1,1]
	v_pk_fma_f32 v[110:111], v[30:31], v[138:139], v[120:121] op_sel_hi:[0,1,1]
	v_pk_fma_f32 v[112:113], v[30:31], v[140:141], v[118:119] op_sel_hi:[0,1,1]
	v_pk_fma_f32 v[114:115], v[30:31], v[148:149], v[124:125] op_sel_hi:[0,1,1]
	v_pk_fma_f32 v[118:119], v[30:31], v[152:153], v[128:129] op_sel_hi:[0,1,1]
	v_pk_fma_f32 v[120:121], v[30:31], v[150:151], v[126:127] op_sel_hi:[0,1,1]
	v_pk_fma_f32 v[54:55], v[30:31], v[54:55], v[108:109] op_sel:[1,0,0]
	v_pk_fma_f32 v[48:49], v[30:31], v[52:53], v[48:49] op_sel:[1,0,0]
	v_pk_fma_f32 v[52:53], v[30:31], v[98:99], v[112:113] op_sel:[1,0,0]
	v_pk_fma_f32 v[96:97], v[30:31], v[96:97], v[110:111] op_sel:[1,0,0]
	v_pk_fma_f32 v[98:99], v[30:31], v[100:101], v[116:117] op_sel:[1,0,0]
	v_pk_fma_f32 v[100:101], v[30:31], v[102:103], v[114:115] op_sel:[1,0,0]
	v_pk_fma_f32 v[102:103], v[30:31], v[104:105], v[120:121] op_sel:[1,0,0]
	v_pk_fma_f32 v[104:105], v[30:31], v[106:107], v[118:119] op_sel:[1,0,0]
	v_mov_b64_e32 v[30:31], v[50:51]
	v_pk_fma_f32 v[48:49], v[68:69], v[48:49], v[80:81]
	v_pk_fma_f32 v[50:51], v[70:71], v[54:55], v[82:83]
	v_pk_fma_f32 v[54:55], v[64:65], v[96:97], v[84:85]
	v_pk_fma_f32 v[52:53], v[66:67], v[52:53], v[88:89]
	v_pk_mul_f32 v[64:65], v[50:51], v[50:51]
	v_pk_mul_f32 v[66:67], v[48:49], v[48:49]
	v_pk_mul_f32 v[68:69], v[52:53], v[52:53]
	v_pk_mul_f32 v[70:71], v[54:55], v[54:55]
	v_pk_fma_f32 v[62:63], v[62:63], v[100:101], v[92:93]
	v_pk_fma_f32 v[60:61], v[60:61], v[98:99], v[86:87]
	v_pk_mov_b32 v[82:83], v[66:67], v[64:65] op_sel:[1,0]
	v_mov_b32_e32 v67, v65
	v_pk_mov_b32 v[64:65], v[70:71], v[68:69] op_sel:[1,0]
	v_mov_b32_e32 v71, v69
	v_pk_fma_f32 v[58:59], v[58:59], v[104:105], v[94:95]
	v_pk_fma_f32 v[56:57], v[56:57], v[102:103], v[90:91]
	v_mul_f32_e32 v74, v61, v61
	v_mul_f32_e32 v80, v63, v63
	v_pk_add_f32 v[66:67], v[82:83], v[66:67]
	v_pk_add_f32 v[64:65], v[64:65], v[70:71]
	v_mul_f32_e32 v84, v56, v56
	v_mul_f32_e32 v85, v57, v57
	v_mul_f32_e32 v86, v58, v58
	v_mul_f32_e32 v87, v59, v59
	v_pk_fma_f32 v[68:69], v[60:61], v[60:61], v[74:75] op_sel_hi:[1,1,0]
	v_pk_fma_f32 v[80:81], v[62:63], v[62:63], v[80:81] op_sel_hi:[1,1,0]
	v_pk_add_f32 v[66:67], v[66:67], v[66:67] op_sel:[0,1] op_sel_hi:[1,0]
	v_pk_add_f32 v[64:65], v[64:65], v[64:65] op_sel:[0,1] op_sel_hi:[1,0]
	v_mov_b32_e32 v69, v86
	v_mov_b32_e32 v81, v87
	v_mov_b32_e32 v67, v84
	v_mov_b32_e32 v65, v85
	v_pk_add_f32 v[68:69], v[68:69], v[80:81]
	v_pk_add_f32 v[64:65], v[66:67], v[64:65]
	s_mov_b32 s62, 34
	v_pk_add_f32 v[64:65], v[64:65], v[68:69]
	s_nop 0
	v_add_f32_e32 v64, v64, v65
	s_nop 1
	v_add_f32_dpp v64, v64, v64 quad_perm:[1,0,3,2] row_mask:0xf bank_mask:0xf bound_ctrl:1
	s_nop 1
	v_add_f32_dpp v64, v64, v64 quad_perm:[2,3,0,1] row_mask:0xf bank_mask:0xf bound_ctrl:1
	s_nop 1
	v_add_f32_dpp v64, v64, v64 row_half_mirror row_mask:0xf bank_mask:0xf bound_ctrl:1
	s_nop 1
	v_add_f32_dpp v64, v64, v64 row_mirror row_mask:0xf bank_mask:0xf bound_ctrl:1
	ds_bpermute_b32 v65, v122, v64
	s_waitcnt lgkmcnt(0)
	v_add_f32_e32 v64, v64, v65
	v_mov_b32_e32 v65, v64
	s_nop 1
	v_permlane32_swap_b32 v65, v64
	s_ashr_i32 s63, s62, 31
	v_add_f32_e32 v64, v65, v64
	v_fmamk_f32 v64, v64, 0x3a800000, v73
	v_mul_f32_e32 v65, 0x4b800000, v64
	v_cmp_gt_f32_e64 s[2:3], s74, v64
	s_lshl_b64 s[10:11], s[62:63], 3
	s_add_u32 s10, s0, s10
	v_cndmask_b32_e64 v64, v64, v65, s[2:3]
	v_rsq_f32_e32 v64, v64
	s_addc_u32 s11, s1, s11
	s_load_dwordx2 s[10:11], s[10:11], 0x0
	s_or_b64 s[6:7], vcc, s[6:7]
	v_mul_f32_e32 v65, 0x45800000, v64
	v_cndmask_b32_e64 v64, v64, v65, s[2:3]
	v_pk_mul_f32 v[48:49], v[48:49], v[64:65] op_sel_hi:[1,0]
	v_pk_mul_f32 v[50:51], v[50:51], v[64:65] op_sel_hi:[1,0]
	s_waitcnt lgkmcnt(0)
	v_lshl_add_u64 v[66:67], s[10:11], 0, v[78:79]
	v_lshl_add_u64 v[78:79], v[78:79], 0, s[4:5]
	v_pk_mul_f32 v[68:69], v[54:55], v[64:65] op_sel_hi:[1,0]
	v_pk_mul_f32 v[52:53], v[52:53], v[64:65] op_sel_hi:[1,0]
	v_pk_mul_f32 v[60:61], v[60:61], v[64:65] op_sel_hi:[1,0]
	v_pk_mul_f32 v[62:63], v[62:63], v[64:65] op_sel_hi:[1,0]
	v_pk_mul_f32 v[70:71], v[56:57], v[64:65] op_sel_hi:[1,0]
	v_pk_mul_f32 v[64:65], v[58:59], v[64:65] op_sel_hi:[1,0]
	v_pk_mul_f32 v[50:51], v[2:3], v[50:51]
	v_pk_mul_f32 v[48:49], v[0:1], v[48:49]
	v_pk_mul_f32 v[54:55], v[6:7], v[52:53]
	v_pk_mul_f32 v[52:53], v[4:5], v[68:69]
	v_pk_mul_f32 v[58:59], v[10:11], v[62:63]
	v_pk_mul_f32 v[56:57], v[8:9], v[60:61]
	v_pk_mul_f32 v[62:63], v[14:15], v[64:65]
	v_pk_mul_f32 v[60:61], v[12:13], v[70:71]
	global_store_dwordx4 v[66:67], v[48:51], off offset:-3072 nt
	global_store_dwordx4 v[66:67], v[52:55], off offset:-2048 nt
	global_store_dwordx4 v[66:67], v[56:59], off offset:-1024 nt
	global_store_dwordx4 v[66:67], v[60:63], off nt
	s_andn2_b64 exec, exec, s[6:7]
	s_cbranch_execnz .LBB0_1977
